# mLSTM item preamble: the four gate-row loads per wave issued together (one memory round trip instead of four)
# speedup vs baseline: 1.0004x; 1.0004x over previous
.LBB0_717:
	v_readfirstlane_b32 s11, v144
	s_and_saveexec_b64 s[26:27], s[42:43]
	ds_write_b32 v109, v1
	s_or_b64 exec, exec, s[26:27]
	s_lshl_b32 s18, s2, 2
	s_and_b32 s18, s18, 28
	s_and_b32 s20, s2, 0xffffffe0
	s_or_b32 s18, s18, s20
	s_bfe_u32 s20, s2, 0x20003
	s_or_b32 s18, s18, s20
	v_readlane_b32 s20, v252, 45
	v_readlane_b32 s21, v252, 46
	s_and_b64 s[20:21], s[20:21], exec
	s_cselect_b32 s18, s18, s2
	s_ashr_i32 s28, s18, 4
	s_ashr_i32 s26, s11, 6
	s_bfe_u32 s20, s18, 0x20002
	s_ashr_i32 s29, s28, 31
	s_cmp_gt_i32 s26, 31
	s_cbranch_scc1 .LBB0_722
	s_ashr_i32 s27, s26, 31
	s_add_i32 s21, s26, -8
	s_lshl_b64 s[30:31], s[28:29], 16
	s_lshl_b64 s[34:35], s[26:27], 11
	s_add_u32 s27, s30, s34
	s_addc_u32 s31, s31, s35
	s_lshl_b32 s30, s20, 2
	s_or_b32 s30, s27, s30
	v_lshl_add_u32 v0, s26, 8, v138
	v_lshl_add_u64 v[2:3], v[96:97], 0, s[30:31]
	v_lshl_add_u64 v[240:241], v[2:3], 0, s[4:5]
	v_lshl_add_u64 v[242:243], v[240:241], 0, s[4:5]
	v_lshl_add_u64 v[244:245], v[242:243], 0, s[4:5]
	global_load_dword v232, v[2:3], off
	global_load_dword v233, v[2:3], off offset:-16
	global_load_dword v234, v[240:241], off
	global_load_dword v235, v[240:241], off offset:-16
	global_load_dword v236, v[242:243], off
	global_load_dword v237, v[242:243], off offset:-16
	global_load_dword v238, v[244:245], off
	global_load_dword v239, v[244:245], off offset:-16
.LBB0_721:
	s_waitcnt vmcnt(0)
	v_mov_b32_e32 v6, v232
	v_mov_b32_e32 v4, v233
	v_mov_b32_e32 v232, v234
	v_mov_b32_e32 v233, v235
	v_mov_b32_e32 v234, v236
	v_mov_b32_e32 v235, v237
	v_mov_b32_e32 v236, v238
	v_mov_b32_e32 v237, v239
	s_add_i32 s21, s21, 8
	s_cmp_gt_i32 s21, 23
	s_waitcnt vmcnt(0) lgkmcnt(0)
	ds_bpermute_b32 v5, v111, v6
	s_waitcnt lgkmcnt(0)
	v_add_f32_e32 v5, v6, v5
	v_cndmask_b32_e64 v5, v5, v6, s[44:45]
	ds_bpermute_b32 v6, v112, v5
	s_waitcnt lgkmcnt(0)
	v_add_f32_e32 v6, v5, v6
	v_cndmask_b32_e64 v5, v6, v5, s[46:47]
	ds_bpermute_b32 v6, v113, v5
	s_waitcnt lgkmcnt(0)
	v_add_f32_e32 v6, v5, v6
	v_cndmask_b32_e64 v5, v6, v5, s[48:49]
	ds_bpermute_b32 v6, v114, v5
	s_waitcnt lgkmcnt(0)
	v_add_f32_e32 v6, v5, v6
	v_cndmask_b32_e64 v5, v6, v5, s[50:51]
	ds_bpermute_b32 v6, v115, v5
	s_waitcnt lgkmcnt(0)
	v_add_f32_e32 v6, v5, v6
	v_cndmask_b32_e64 v5, v6, v5, s[52:53]
	ds_bpermute_b32 v6, v116, v5
	s_waitcnt lgkmcnt(0)
	v_add_f32_e32 v6, v5, v6
	v_cndmask_b32_e64 v5, v6, v5, s[54:55]
	v_sub_f32_e32 v4, v4, v5
	ds_bpermute_b32 v6, v111, v4
	ds_write2st64_b32 v0, v4, v5 offset1:32
	s_waitcnt lgkmcnt(1)
	v_max_f32_e32 v6, v6, v6
	v_max_f32_e32 v6, v4, v6
	v_cndmask_b32_e64 v6, v6, v4, s[44:45]
	ds_bpermute_b32 v7, v112, v6
	s_waitcnt lgkmcnt(0)
	v_max_f32_e32 v7, v7, v7
	v_max_f32_e32 v7, v6, v7
	v_cndmask_b32_e64 v6, v7, v6, s[46:47]
	ds_bpermute_b32 v7, v113, v6
	s_waitcnt lgkmcnt(0)
	v_max_f32_e32 v7, v7, v7
	v_max_f32_e32 v7, v6, v7
	v_cndmask_b32_e64 v6, v7, v6, s[48:49]
	ds_bpermute_b32 v7, v114, v6
	s_waitcnt lgkmcnt(0)
	v_max_f32_e32 v7, v7, v7
	v_max_f32_e32 v7, v6, v7
	v_cndmask_b32_e64 v6, v7, v6, s[50:51]
	ds_bpermute_b32 v7, v115, v6
	s_waitcnt lgkmcnt(0)
	v_max_f32_e32 v7, v7, v7
	v_max_f32_e32 v7, v6, v7
	v_cndmask_b32_e64 v6, v7, v6, s[52:53]
	ds_bpermute_b32 v7, v116, v6
	v_max_f32_e32 v4, v6, v6
	s_waitcnt lgkmcnt(0)
	v_max_f32_e32 v5, v7, v7
	v_max_f32_e32 v4, v4, v5
	v_cndmask_b32_e64 v4, v4, v6, s[54:55]
	ds_write_b32 v0, v4 offset:16384
	v_add_u32_e32 v0, 0x800, v0
	s_cbranch_scc0 .LBB0_721
